# conv item order: k-block fastest (8 waves write 1 KB contiguous per output row), otherwise as v30
# baseline (speedup 1.0000x reference)
.Lconv_entry:
	v_readlane_b32 s0, v255, 7
	s_and_b32 s1, s76, 31
	s_lshl_b32 s1, s1, 3
	s_lshr_b32 s2, s76, 5
	s_or_b32 s1, s1, s2
	s_mul_i32 s2, s1, 0x9d
	s_sub_u32 s3, s1, 0x90
	s_mul_i32 s3, s3, 0xed
	s_add_u32 s3, s3, 0x5850
	s_movk_i32 s15, 0xed
	s_cmp_lt_u32 s1, 0x90
	s_cselect_b32 s14, s2, s3
	s_cselect_b32 s15, 0x9d, s15
	s_add_u32 s15, s15, s14
	s_add_u32 s14, s14, s0
	v_lshrrev_b32_e32 v2, 3, v254
	v_lshlrev_b32_e32 v2, 4, v2
	v_and_b32_e32 v3, 7, v254
	v_lshlrev_b32_e32 v4, 4, v3
	v_lshlrev_b32_e32 v3, 2, v3
	v_mov_b32_e32 v5, 0x43e00000
	s_mov_b32 s25, 0xc3e00000
	s_cmp_lt_u32 s14, s15
	s_cbranch_scc0 .Lconv_done
	s_cmp_lt_u32 s14, 0x8000
	s_cbranch_scc0 .Lconv_dn_p
	s_lshr_b32 s0, s14, 14
	s_and_b32 s1, s14, 0x3fff
	s_cmp_eq_u32 s0, 0
	s_cselect_b32 s16, s36, s38
	s_cselect_b32 s17, s37, s39
	s_lshr_b32 s2, s1, 8
	s_and_b32 s3, s1, 0xff
	s_and_b32 s1, s3, 15
	s_lshr_b32 s3, s3, 4
	s_lshl_b32 s10, s2, 22
	s_lshl_b32 s11, s1, 18
	s_add_u32 s10, s10, s11
	s_lshl_b32 s11, s3, 7
	s_add_u32 s10, s10, s11
	s_add_u32 s16, s16, s10
	s_addc_u32 s17, s17, 0
	s_movk_i32 s18, 0x800
	s_lshl_b32 s10, s2, 10
	s_lshr_b32 s11, s3, 2
	s_lshl_b32 s11, s11, 8
	s_add_u32 s10, s10, s11
	s_lshl_b32 s11, s0, 7
	s_add_u32 s10, s10, s11
	s_and_b32 s11, s3, 3
	s_lshl_b32 s11, s11, 5
	s_add_u32 s10, s10, s11
	s_lshl_b32 s10, s10, 11
	s_lshl_b32 s11, s1, 7
	s_add_u32 s10, s10, s11
	s_add_u32 s20, s50, 0x1c200000
	s_addc_u32 s21, s51, 0
	s_add_u32 s20, s20, s10
	s_addc_u32 s21, s21, 0
	s_movk_i32 s19, 0x800
	s_branch .Lconv_ad_p
.Lconv_dn_p:
	s_sub_u32 s1, s14, 0x8000
	s_lshr_b32 s2, s1, 8
	s_and_b32 s3, s1, 0xff
	s_and_b32 s1, s3, 3
	s_lshr_b32 s3, s3, 2
	s_lshl_b32 s10, s2, 22
	s_lshl_b32 s11, s1, 20
	s_add_u32 s10, s10, s11
	s_lshl_b32 s11, s3, 7
	s_add_u32 s10, s10, s11
	s_add_u32 s16, s40, s10
	s_addc_u32 s17, s41, 0
	s_movk_i32 s18, 0x2000
	s_lshl_b32 s10, s2, 11
	s_lshl_b32 s11, s3, 5
	s_add_u32 s10, s10, s11
	s_lshl_b32 s10, s10, 9
	s_lshl_b32 s11, s1, 7
	s_add_u32 s10, s10, s11
	s_add_u32 s20, s50, 0x2c600000
	s_addc_u32 s21, s51, 0
	s_add_u32 s20, s20, s10
	s_addc_u32 s21, s21, 0
	s_movk_i32 s19, 0x200

.Lconv_loop:
	s_add_u32 s27, s14, 8
	s_cmp_lt_u32 s27, s15
	s_cbranch_scc0 .Lconv_tailA
	s_cmp_lt_u32 s27, 0x8000
	s_cbranch_scc0 .Lconv_dn_b
	s_lshr_b32 s0, s27, 14
	s_and_b32 s1, s27, 0x3fff
	s_cmp_eq_u32 s0, 0
	s_cselect_b32 s16, s36, s38
	s_cselect_b32 s17, s37, s39
	s_lshr_b32 s2, s1, 8
	s_and_b32 s3, s1, 0xff
	s_and_b32 s1, s3, 15
	s_lshr_b32 s3, s3, 4
	s_lshl_b32 s10, s2, 22
	s_lshl_b32 s11, s1, 18
	s_add_u32 s10, s10, s11
	s_lshl_b32 s11, s3, 7
	s_add_u32 s10, s10, s11
	s_add_u32 s16, s16, s10
	s_addc_u32 s17, s17, 0
	s_movk_i32 s18, 0x800
	s_lshl_b32 s10, s2, 10
	s_lshr_b32 s11, s3, 2
	s_lshl_b32 s11, s11, 8
	s_add_u32 s10, s10, s11
	s_lshl_b32 s11, s0, 7
	s_add_u32 s10, s10, s11
	s_and_b32 s11, s3, 3
	s_lshl_b32 s11, s11, 5
	s_add_u32 s10, s10, s11
	s_lshl_b32 s10, s10, 11
	s_lshl_b32 s11, s1, 7
	s_add_u32 s10, s10, s11
	s_add_u32 s22, s50, 0x1c200000
	s_addc_u32 s23, s51, 0
	s_add_u32 s22, s22, s10
	s_addc_u32 s23, s23, 0
	s_movk_i32 s24, 0x800
	s_branch .Lconv_ad_b
.Lconv_dn_b:
	s_sub_u32 s1, s27, 0x8000
	s_lshr_b32 s2, s1, 8
	s_and_b32 s3, s1, 0xff
	s_and_b32 s1, s3, 3
	s_lshr_b32 s3, s3, 2
	s_lshl_b32 s10, s2, 22
	s_lshl_b32 s11, s1, 20
	s_add_u32 s10, s10, s11
	s_lshl_b32 s11, s3, 7
	s_add_u32 s10, s10, s11
	s_add_u32 s16, s40, s10
	s_addc_u32 s17, s41, 0
	s_movk_i32 s18, 0x2000
	s_lshl_b32 s10, s2, 11
	s_lshl_b32 s11, s3, 5
	s_add_u32 s10, s10, s11
	s_lshl_b32 s10, s10, 9
	s_lshl_b32 s11, s1, 7
	s_add_u32 s10, s10, s11
	s_add_u32 s22, s50, 0x2c600000
	s_addc_u32 s23, s51, 0
	s_add_u32 s22, s22, s10
	s_addc_u32 s23, s23, 0
	s_movk_i32 s24, 0x200
.Lconv_ad_b:
	v_mad_u32_u24 v6, v2, s18, v4
	v_mad_u32_u24 v8, v3, s24, v2
	global_load_dwordx4 v[80:83], v6, s[16:17] nt
	s_add_u32 s16, s16, s18
	s_addc_u32 s17, s17, 0
	global_load_dwordx4 v[84:87], v6, s[16:17] nt
	s_add_u32 s16, s16, s18
	s_addc_u32 s17, s17, 0
	global_load_dwordx4 v[88:91], v6, s[16:17] nt
	s_add_u32 s16, s16, s18
	s_addc_u32 s17, s17, 0
	global_load_dwordx4 v[92:95], v6, s[16:17] nt
	s_add_u32 s16, s16, s18
	s_addc_u32 s17, s17, 0
	global_load_dwordx4 v[96:99], v6, s[16:17] nt
	s_add_u32 s16, s16, s18
	s_addc_u32 s17, s17, 0
	global_load_dwordx4 v[100:103], v6, s[16:17] nt
	s_add_u32 s16, s16, s18
	s_addc_u32 s17, s17, 0
	global_load_dwordx4 v[104:107], v6, s[16:17] nt
	s_add_u32 s16, s16, s18
	s_addc_u32 s17, s17, 0
	global_load_dwordx4 v[108:111], v6, s[16:17] nt
	s_add_u32 s16, s16, s18
	s_addc_u32 s17, s17, 0
	global_load_dwordx4 v[112:115], v6, s[16:17] nt
	s_add_u32 s16, s16, s18
	s_addc_u32 s17, s17, 0
	global_load_dwordx4 v[116:119], v6, s[16:17] nt
	s_add_u32 s16, s16, s18
	s_addc_u32 s17, s17, 0
	global_load_dwordx4 v[120:123], v6, s[16:17] nt
	s_add_u32 s16, s16, s18
	s_addc_u32 s17, s17, 0
	global_load_dwordx4 v[124:127], v6, s[16:17] nt
	s_add_u32 s16, s16, s18
	s_addc_u32 s17, s17, 0
	global_load_dwordx4 v[128:131], v6, s[16:17] nt
	s_add_u32 s16, s16, s18
	s_addc_u32 s17, s17, 0
	global_load_dwordx4 v[132:135], v6, s[16:17] nt
	s_add_u32 s16, s16, s18
	s_addc_u32 s17, s17, 0
	global_load_dwordx4 v[136:139], v6, s[16:17] nt
	s_add_u32 s16, s16, s18
	s_addc_u32 s17, s17, 0
	global_load_dwordx4 v[140:143], v6, s[16:17] nt
	s_waitcnt vmcnt(16)
	v_mul_f32_e32 v160, 0x41800000, v16
	v_mul_f32_e32 v161, 0x41800000, v20
	v_mul_f32_e32 v162, 0x41800000, v24
	v_mul_f32_e32 v163, 0x41800000, v28
	v_med3_f32 v160, v160, s25, v5
	v_med3_f32 v161, v161, s25, v5
	v_med3_f32 v162, v162, s25, v5
	v_med3_f32 v163, v163, s25, v5
	v_cvt_pk_fp8_f32 v144, v160, v161
	v_cvt_pk_fp8_f32 v144, v162, v163 op_sel:[0,0,1]
	v_mul_f32_e32 v164, 0x41800000, v32
	v_mul_f32_e32 v165, 0x41800000, v36
	v_mul_f32_e32 v166, 0x41800000, v40
	v_mul_f32_e32 v167, 0x41800000, v44
	v_med3_f32 v164, v164, s25, v5
	v_med3_f32 v165, v165, s25, v5
	v_med3_f32 v166, v166, s25, v5
	v_med3_f32 v167, v167, s25, v5
	v_cvt_pk_fp8_f32 v145, v164, v165
	v_cvt_pk_fp8_f32 v145, v166, v167 op_sel:[0,0,1]
	v_mul_f32_e32 v160, 0x41800000, v48
	v_mul_f32_e32 v161, 0x41800000, v52
	v_mul_f32_e32 v162, 0x41800000, v56
	v_mul_f32_e32 v163, 0x41800000, v60
	v_med3_f32 v160, v160, s25, v5
	v_med3_f32 v161, v161, s25, v5
	v_med3_f32 v162, v162, s25, v5
	v_med3_f32 v163, v163, s25, v5
	v_cvt_pk_fp8_f32 v146, v160, v161
	v_cvt_pk_fp8_f32 v146, v162, v163 op_sel:[0,0,1]
	v_mul_f32_e32 v164, 0x41800000, v64
	v_mul_f32_e32 v165, 0x41800000, v68
	v_mul_f32_e32 v166, 0x41800000, v72
	v_mul_f32_e32 v167, 0x41800000, v76
	v_med3_f32 v164, v164, s25, v5
	v_med3_f32 v165, v165, s25, v5
	v_med3_f32 v166, v166, s25, v5
	v_med3_f32 v167, v167, s25, v5
	v_cvt_pk_fp8_f32 v147, v164, v165
	v_cvt_pk_fp8_f32 v147, v166, v167 op_sel:[0,0,1]
	s_nop 0
	global_store_dwordx4 v7, v[144:147], s[20:21] nt
	s_add_u32 s20, s20, s19
	s_addc_u32 s21, s21, 0
	v_mul_f32_e32 v160, 0x41800000, v17
	v_mul_f32_e32 v161, 0x41800000, v21
	v_mul_f32_e32 v162, 0x41800000, v25
	v_mul_f32_e32 v163, 0x41800000, v29
	v_med3_f32 v160, v160, s25, v5
	v_med3_f32 v161, v161, s25, v5
	v_med3_f32 v162, v162, s25, v5
	v_med3_f32 v163, v163, s25, v5
	v_cvt_pk_fp8_f32 v148, v160, v161
	v_cvt_pk_fp8_f32 v148, v162, v163 op_sel:[0,0,1]
	v_mul_f32_e32 v164, 0x41800000, v33
	v_mul_f32_e32 v165, 0x41800000, v37
	v_mul_f32_e32 v166, 0x41800000, v41
	v_mul_f32_e32 v167, 0x41800000, v45
	v_med3_f32 v164, v164, s25, v5
	v_med3_f32 v165, v165, s25, v5
	v_med3_f32 v166, v166, s25, v5
	v_med3_f32 v167, v167, s25, v5
	v_cvt_pk_fp8_f32 v149, v164, v165
	v_cvt_pk_fp8_f32 v149, v166, v167 op_sel:[0,0,1]
	v_mul_f32_e32 v160, 0x41800000, v49
	v_mul_f32_e32 v161, 0x41800000, v53
	v_mul_f32_e32 v162, 0x41800000, v57
	v_mul_f32_e32 v163, 0x41800000, v61
	v_med3_f32 v160, v160, s25, v5
	v_med3_f32 v161, v161, s25, v5
	v_med3_f32 v162, v162, s25, v5
	v_med3_f32 v163, v163, s25, v5
	v_cvt_pk_fp8_f32 v150, v160, v161
	v_cvt_pk_fp8_f32 v150, v162, v163 op_sel:[0,0,1]
	v_mul_f32_e32 v164, 0x41800000, v65
	v_mul_f32_e32 v165, 0x41800000, v69
	v_mul_f32_e32 v166, 0x41800000, v73
	v_mul_f32_e32 v167, 0x41800000, v77
	v_med3_f32 v164, v164, s25, v5
	v_med3_f32 v165, v165, s25, v5
	v_med3_f32 v166, v166, s25, v5
	v_med3_f32 v167, v167, s25, v5
	v_cvt_pk_fp8_f32 v151, v164, v165
	v_cvt_pk_fp8_f32 v151, v166, v167 op_sel:[0,0,1]
	s_nop 0
	global_store_dwordx4 v7, v[148:151], s[20:21] nt
	s_add_u32 s20, s20, s19
	s_addc_u32 s21, s21, 0
	v_mul_f32_e32 v160, 0x41800000, v18
	v_mul_f32_e32 v161, 0x41800000, v22
	v_mul_f32_e32 v162, 0x41800000, v26
	v_mul_f32_e32 v163, 0x41800000, v30
	v_med3_f32 v160, v160, s25, v5
	v_med3_f32 v161, v161, s25, v5
	v_med3_f32 v162, v162, s25, v5
	v_med3_f32 v163, v163, s25, v5
	v_cvt_pk_fp8_f32 v152, v160, v161
	v_cvt_pk_fp8_f32 v152, v162, v163 op_sel:[0,0,1]
	v_mul_f32_e32 v164, 0x41800000, v34
	v_mul_f32_e32 v165, 0x41800000, v38
	v_mul_f32_e32 v166, 0x41800000, v42
	v_mul_f32_e32 v167, 0x41800000, v46
	v_med3_f32 v164, v164, s25, v5
	v_med3_f32 v165, v165, s25, v5
	v_med3_f32 v166, v166, s25, v5
	v_med3_f32 v167, v167, s25, v5
	v_cvt_pk_fp8_f32 v153, v164, v165
	v_cvt_pk_fp8_f32 v153, v166, v167 op_sel:[0,0,1]
	v_mul_f32_e32 v160, 0x41800000, v50
	v_mul_f32_e32 v161, 0x41800000, v54
	v_mul_f32_e32 v162, 0x41800000, v58
	v_mul_f32_e32 v163, 0x41800000, v62
	v_med3_f32 v160, v160, s25, v5
	v_med3_f32 v161, v161, s25, v5
	v_med3_f32 v162, v162, s25, v5
	v_med3_f32 v163, v163, s25, v5
	v_cvt_pk_fp8_f32 v154, v160, v161
	v_cvt_pk_fp8_f32 v154, v162, v163 op_sel:[0,0,1]
	v_mul_f32_e32 v164, 0x41800000, v66
	v_mul_f32_e32 v165, 0x41800000, v70
	v_mul_f32_e32 v166, 0x41800000, v74
	v_mul_f32_e32 v167, 0x41800000, v78
	v_med3_f32 v164, v164, s25, v5
	v_med3_f32 v165, v165, s25, v5
	v_med3_f32 v166, v166, s25, v5
	v_med3_f32 v167, v167, s25, v5
	v_cvt_pk_fp8_f32 v155, v164, v165
	v_cvt_pk_fp8_f32 v155, v166, v167 op_sel:[0,0,1]
	s_nop 0
	global_store_dwordx4 v7, v[152:155], s[20:21] nt
	s_add_u32 s20, s20, s19
	s_addc_u32 s21, s21, 0
	v_mul_f32_e32 v160, 0x41800000, v19
	v_mul_f32_e32 v161, 0x41800000, v23
	v_mul_f32_e32 v162, 0x41800000, v27
	v_mul_f32_e32 v163, 0x41800000, v31
	v_med3_f32 v160, v160, s25, v5
	v_med3_f32 v161, v161, s25, v5
	v_med3_f32 v162, v162, s25, v5
	v_med3_f32 v163, v163, s25, v5
	v_cvt_pk_fp8_f32 v156, v160, v161
	v_cvt_pk_fp8_f32 v156, v162, v163 op_sel:[0,0,1]
	v_mul_f32_e32 v164, 0x41800000, v35
	v_mul_f32_e32 v165, 0x41800000, v39
	v_mul_f32_e32 v166, 0x41800000, v43
	v_mul_f32_e32 v167, 0x41800000, v47
	v_med3_f32 v164, v164, s25, v5
	v_med3_f32 v165, v165, s25, v5
	v_med3_f32 v166, v166, s25, v5
	v_med3_f32 v167, v167, s25, v5
	v_cvt_pk_fp8_f32 v157, v164, v165
	v_cvt_pk_fp8_f32 v157, v166, v167 op_sel:[0,0,1]
	v_mul_f32_e32 v160, 0x41800000, v51
	v_mul_f32_e32 v161, 0x41800000, v55
	v_mul_f32_e32 v162, 0x41800000, v59
	v_mul_f32_e32 v163, 0x41800000, v63
	v_med3_f32 v160, v160, s25, v5
	v_med3_f32 v161, v161, s25, v5
	v_med3_f32 v162, v162, s25, v5
	v_med3_f32 v163, v163, s25, v5
	v_cvt_pk_fp8_f32 v158, v160, v161
	v_cvt_pk_fp8_f32 v158, v162, v163 op_sel:[0,0,1]
	v_mul_f32_e32 v164, 0x41800000, v67
	v_mul_f32_e32 v165, 0x41800000, v71
	v_mul_f32_e32 v166, 0x41800000, v75
	v_mul_f32_e32 v167, 0x41800000, v79
	v_med3_f32 v164, v164, s25, v5
	v_med3_f32 v165, v165, s25, v5
	v_med3_f32 v166, v166, s25, v5
	v_med3_f32 v167, v167, s25, v5
	v_cvt_pk_fp8_f32 v159, v164, v165
	v_cvt_pk_fp8_f32 v159, v166, v167 op_sel:[0,0,1]
	s_nop 0
	global_store_dwordx4 v7, v[156:159], s[20:21] nt
	s_add_u32 s14, s27, 8
	s_cmp_lt_u32 s14, s15
	s_cbranch_scc0 .Lconv_tailB
	s_cmp_lt_u32 s14, 0x8000
	s_cbranch_scc0 .Lconv_dn_a
	s_lshr_b32 s0, s14, 14
	s_and_b32 s1, s14, 0x3fff
	s_cmp_eq_u32 s0, 0
	s_cselect_b32 s16, s36, s38
	s_cselect_b32 s17, s37, s39
	s_lshr_b32 s2, s1, 8
	s_and_b32 s3, s1, 0xff
	s_and_b32 s1, s3, 15
	s_lshr_b32 s3, s3, 4
	s_lshl_b32 s10, s2, 22
	s_lshl_b32 s11, s1, 18
	s_add_u32 s10, s10, s11
	s_lshl_b32 s11, s3, 7
	s_add_u32 s10, s10, s11
	s_add_u32 s16, s16, s10
	s_addc_u32 s17, s17, 0
	s_movk_i32 s18, 0x800
	s_lshl_b32 s10, s2, 10
	s_lshr_b32 s11, s3, 2
	s_lshl_b32 s11, s11, 8
	s_add_u32 s10, s10, s11
	s_lshl_b32 s11, s0, 7
	s_add_u32 s10, s10, s11
	s_and_b32 s11, s3, 3
	s_lshl_b32 s11, s11, 5
	s_add_u32 s10, s10, s11
	s_lshl_b32 s10, s10, 11
	s_lshl_b32 s11, s1, 7
	s_add_u32 s10, s10, s11
	s_add_u32 s20, s50, 0x1c200000
	s_addc_u32 s21, s51, 0
	s_add_u32 s20, s20, s10
	s_addc_u32 s21, s21, 0
	s_movk_i32 s19, 0x800
	s_branch .Lconv_ad_a
